# expert weight conversion hosted in the attention phase: all 64 row loads of a tile issued before the K/V staging
# speedup vs baseline: 1.0517x; 1.0019x over previous
.Lp2w_go_a:
	v_readlane_b32 s62, v239, 44
	v_readlane_b32 s63, v239, 45
	s_add_u32 s100, s82, s30
	s_addc_u32 s101, s83, 0
	s_add_u32 s70, s62, s31
	s_addc_u32 s71, s63, 0
	global_load_dword v34, v178, s[100:101] nt
	s_add_u32 s100, s100, s97
	s_addc_u32 s101, s101, 0
	global_load_dword v35, v178, s[100:101] nt
	s_add_u32 s100, s100, s97
	s_addc_u32 s101, s101, 0
	global_load_dword v36, v178, s[100:101] nt
	s_add_u32 s100, s100, s97
	s_addc_u32 s101, s101, 0
	global_load_dword v37, v178, s[100:101] nt
	s_add_u32 s100, s100, s97
	s_addc_u32 s101, s101, 0
	global_load_dword v38, v178, s[100:101] nt
	s_add_u32 s100, s100, s97
	s_addc_u32 s101, s101, 0
	global_load_dword v39, v178, s[100:101] nt
	s_add_u32 s100, s100, s97
	s_addc_u32 s101, s101, 0
	global_load_dword v40, v178, s[100:101] nt
	s_add_u32 s100, s100, s97
	s_addc_u32 s101, s101, 0
	global_load_dword v41, v178, s[100:101] nt
	s_add_u32 s100, s100, s97
	s_addc_u32 s101, s101, 0
	global_load_dword v42, v178, s[100:101] nt
	s_add_u32 s100, s100, s97
	s_addc_u32 s101, s101, 0
	global_load_dword v43, v178, s[100:101] nt
	s_add_u32 s100, s100, s97
	s_addc_u32 s101, s101, 0
	global_load_dword v44, v178, s[100:101] nt
	s_add_u32 s100, s100, s97
	s_addc_u32 s101, s101, 0
	global_load_dword v45, v178, s[100:101] nt
	s_add_u32 s100, s100, s97
	s_addc_u32 s101, s101, 0
	global_load_dword v46, v178, s[100:101] nt
	s_add_u32 s100, s100, s97
	s_addc_u32 s101, s101, 0
	global_load_dword v47, v178, s[100:101] nt
	s_add_u32 s100, s100, s97
	s_addc_u32 s101, s101, 0
	global_load_dword v48, v178, s[100:101] nt
	s_add_u32 s100, s100, s97
	s_addc_u32 s101, s101, 0
	global_load_dword v49, v178, s[100:101] nt
	s_add_u32 s100, s100, s97
	s_addc_u32 s101, s101, 0
	global_load_dword v50, v178, s[100:101] nt
	s_add_u32 s100, s100, s97
	s_addc_u32 s101, s101, 0
	global_load_dword v51, v178, s[100:101] nt
	s_add_u32 s100, s100, s97
	s_addc_u32 s101, s101, 0
	global_load_dword v52, v178, s[100:101] nt
	s_add_u32 s100, s100, s97
	s_addc_u32 s101, s101, 0
	global_load_dword v53, v178, s[100:101] nt
	s_add_u32 s100, s100, s97
	s_addc_u32 s101, s101, 0
	global_load_dword v54, v178, s[100:101] nt
	s_add_u32 s100, s100, s97
	s_addc_u32 s101, s101, 0
	global_load_dword v55, v178, s[100:101] nt
	s_add_u32 s100, s100, s97
	s_addc_u32 s101, s101, 0
	global_load_dword v56, v178, s[100:101] nt
	s_add_u32 s100, s100, s97
	s_addc_u32 s101, s101, 0
	global_load_dword v57, v178, s[100:101] nt
	s_add_u32 s100, s100, s97
	s_addc_u32 s101, s101, 0
	global_load_dword v58, v178, s[100:101] nt
	s_add_u32 s100, s100, s97
	s_addc_u32 s101, s101, 0
	global_load_dword v59, v178, s[100:101] nt
	s_add_u32 s100, s100, s97
	s_addc_u32 s101, s101, 0
	global_load_dword v60, v178, s[100:101] nt
	s_add_u32 s100, s100, s97
	s_addc_u32 s101, s101, 0
	global_load_dword v61, v178, s[100:101] nt
	s_add_u32 s100, s100, s97
	s_addc_u32 s101, s101, 0
	global_load_dword v62, v178, s[100:101] nt
	s_add_u32 s100, s100, s97
	s_addc_u32 s101, s101, 0
	global_load_dword v63, v178, s[100:101] nt
	s_add_u32 s100, s100, s97
	s_addc_u32 s101, s101, 0
	global_load_dword v64, v178, s[100:101] nt
	s_add_u32 s100, s100, s97
	s_addc_u32 s101, s101, 0
	global_load_dword v65, v178, s[100:101] nt
	s_add_u32 s100, s100, s97
	s_addc_u32 s101, s101, 0
	global_load_dword v66, v178, s[100:101] nt
	s_add_u32 s100, s100, s97
	s_addc_u32 s101, s101, 0
	global_load_dword v67, v178, s[100:101] nt
	s_add_u32 s100, s100, s97
	s_addc_u32 s101, s101, 0
	global_load_dword v68, v178, s[100:101] nt
	s_add_u32 s100, s100, s97
	s_addc_u32 s101, s101, 0
	global_load_dword v69, v178, s[100:101] nt
	s_add_u32 s100, s100, s97
	s_addc_u32 s101, s101, 0
	global_load_dword v70, v178, s[100:101] nt
	s_add_u32 s100, s100, s97
	s_addc_u32 s101, s101, 0
	global_load_dword v71, v178, s[100:101] nt
	s_add_u32 s100, s100, s97
	s_addc_u32 s101, s101, 0
	global_load_dword v72, v178, s[100:101] nt
	s_add_u32 s100, s100, s97
	s_addc_u32 s101, s101, 0
	global_load_dword v73, v178, s[100:101] nt
	s_add_u32 s100, s100, s97
	s_addc_u32 s101, s101, 0
	global_load_dword v74, v178, s[100:101] nt
	s_add_u32 s100, s100, s97
	s_addc_u32 s101, s101, 0
	global_load_dword v75, v178, s[100:101] nt
	s_add_u32 s100, s100, s97
	s_addc_u32 s101, s101, 0
	global_load_dword v76, v178, s[100:101] nt
	s_add_u32 s100, s100, s97
	s_addc_u32 s101, s101, 0
	global_load_dword v77, v178, s[100:101] nt
	s_add_u32 s100, s100, s97
	s_addc_u32 s101, s101, 0
	global_load_dword v78, v178, s[100:101] nt
	s_add_u32 s100, s100, s97
	s_addc_u32 s101, s101, 0
	global_load_dword v79, v178, s[100:101] nt
	s_add_u32 s100, s100, s97
	s_addc_u32 s101, s101, 0
	global_load_dword v80, v178, s[100:101] nt
	s_add_u32 s100, s100, s97
	s_addc_u32 s101, s101, 0
	global_load_dword v81, v178, s[100:101] nt
	s_add_u32 s100, s100, s97
	s_addc_u32 s101, s101, 0
	global_load_dword v82, v178, s[100:101] nt
	s_add_u32 s100, s100, s97
	s_addc_u32 s101, s101, 0
	global_load_dword v83, v178, s[100:101] nt
	s_add_u32 s100, s100, s97
	s_addc_u32 s101, s101, 0
	global_load_dword v84, v178, s[100:101] nt
	s_add_u32 s100, s100, s97
	s_addc_u32 s101, s101, 0
	global_load_dword v85, v178, s[100:101] nt
	s_add_u32 s100, s100, s97
	s_addc_u32 s101, s101, 0
	global_load_dword v86, v178, s[100:101] nt
	s_add_u32 s100, s100, s97
	s_addc_u32 s101, s101, 0
	global_load_dword v87, v178, s[100:101] nt
	s_add_u32 s100, s100, s97
	s_addc_u32 s101, s101, 0
	global_load_dword v88, v178, s[100:101] nt
	s_add_u32 s100, s100, s97
	s_addc_u32 s101, s101, 0
	global_load_dword v89, v178, s[100:101] nt
	s_add_u32 s100, s100, s97
	s_addc_u32 s101, s101, 0
	global_load_dword v90, v178, s[100:101] nt
	s_add_u32 s100, s100, s97
	s_addc_u32 s101, s101, 0
	global_load_dword v91, v178, s[100:101] nt
	s_add_u32 s100, s100, s97
	s_addc_u32 s101, s101, 0
	global_load_dword v92, v178, s[100:101] nt
	s_add_u32 s100, s100, s97
	s_addc_u32 s101, s101, 0
	global_load_dword v93, v178, s[100:101] nt
	s_add_u32 s100, s100, s97
	s_addc_u32 s101, s101, 0
	global_load_dword v94, v178, s[100:101] nt
	s_add_u32 s100, s100, s97
	s_addc_u32 s101, s101, 0
	global_load_dword v95, v178, s[100:101] nt
	s_add_u32 s100, s100, s97
	s_addc_u32 s101, s101, 0
	global_load_dword v96, v178, s[100:101] nt
	s_add_u32 s100, s100, s97
	s_addc_u32 s101, s101, 0
	s_waitcnt vmcnt(63)
	global_load_dword v97, v178, s[100:101] nt
	s_add_u32 s100, s100, s97
	s_addc_u32 s101, s101, 0
	s_branch .Lp2w_x_done

.LBB0_266:
	s_add_i32 s60, s60, s74
	s_cmpk_lt_i32 s60, 0x1000
	s_waitcnt lgkmcnt(0)
	s_barrier
	s_cselect_b64 s[90:91], -1, 0
	s_cmpk_gt_i32 s60, 0xfff
	s_cselect_b64 s[64:65], -1, 0
	s_cmp_eq_u32 s99, 0
	s_cbranch_scc1 .Lp2w_y_skip
	s_waitcnt vmcnt(48)
	v_mul_f32_e32 v34, 0x42000000, v34
	v_mul_f32_e32 v35, 0x42000000, v35
	v_mul_f32_e32 v36, 0x42000000, v36
	v_mul_f32_e32 v37, 0x42000000, v37
	v_mul_f32_e32 v38, 0x42000000, v38
	v_mul_f32_e32 v39, 0x42000000, v39
	v_mul_f32_e32 v40, 0x42000000, v40
	v_mul_f32_e32 v41, 0x42000000, v41
	v_mul_f32_e32 v42, 0x42000000, v42
	v_mul_f32_e32 v43, 0x42000000, v43
	v_mul_f32_e32 v44, 0x42000000, v44
	v_mul_f32_e32 v45, 0x42000000, v45
	v_mul_f32_e32 v46, 0x42000000, v46
	v_mul_f32_e32 v47, 0x42000000, v47
	v_mul_f32_e32 v48, 0x42000000, v48
	v_mul_f32_e32 v49, 0x42000000, v49
	v_cvt_pk_fp8_f32 v154, v34, v35
	v_cvt_pk_fp8_f32 v155, v38, v39
	v_cvt_pk_fp8_f32 v156, v42, v43
	v_cvt_pk_fp8_f32 v157, v46, v47
	v_cvt_pk_fp8_f32 v154, v36, v37 op_sel:[0,0,1]
	v_cvt_pk_fp8_f32 v155, v40, v41 op_sel:[0,0,1]
	v_cvt_pk_fp8_f32 v156, v44, v45 op_sel:[0,0,1]
	v_cvt_pk_fp8_f32 v157, v48, v49 op_sel:[0,0,1]
	s_waitcnt vmcnt(32)
	v_mul_f32_e32 v50, 0x42000000, v50
	v_mul_f32_e32 v51, 0x42000000, v51
	v_mul_f32_e32 v52, 0x42000000, v52
	v_mul_f32_e32 v53, 0x42000000, v53
	v_mul_f32_e32 v54, 0x42000000, v54
	v_mul_f32_e32 v55, 0x42000000, v55
	v_mul_f32_e32 v56, 0x42000000, v56
	v_mul_f32_e32 v57, 0x42000000, v57
	v_mul_f32_e32 v58, 0x42000000, v58
	v_mul_f32_e32 v59, 0x42000000, v59
	v_mul_f32_e32 v60, 0x42000000, v60
	v_mul_f32_e32 v61, 0x42000000, v61
	v_mul_f32_e32 v62, 0x42000000, v62
	v_mul_f32_e32 v63, 0x42000000, v63
	v_mul_f32_e32 v64, 0x42000000, v64
	v_mul_f32_e32 v65, 0x42000000, v65
	v_cvt_pk_fp8_f32 v158, v50, v51
	v_cvt_pk_fp8_f32 v159, v54, v55
	v_cvt_pk_fp8_f32 v160, v58, v59
	v_cvt_pk_fp8_f32 v161, v62, v63
	v_cvt_pk_fp8_f32 v158, v52, v53 op_sel:[0,0,1]
	v_cvt_pk_fp8_f32 v159, v56, v57 op_sel:[0,0,1]
	v_cvt_pk_fp8_f32 v160, v60, v61 op_sel:[0,0,1]
	v_cvt_pk_fp8_f32 v161, v64, v65 op_sel:[0,0,1]
	s_waitcnt vmcnt(16)
	v_mul_f32_e32 v66, 0x42000000, v66
	v_mul_f32_e32 v67, 0x42000000, v67
	v_mul_f32_e32 v68, 0x42000000, v68
	v_mul_f32_e32 v69, 0x42000000, v69
	v_mul_f32_e32 v70, 0x42000000, v70
	v_mul_f32_e32 v71, 0x42000000, v71
	v_mul_f32_e32 v72, 0x42000000, v72
	v_mul_f32_e32 v73, 0x42000000, v73
	v_mul_f32_e32 v74, 0x42000000, v74
	v_mul_f32_e32 v75, 0x42000000, v75
	v_mul_f32_e32 v76, 0x42000000, v76
	v_mul_f32_e32 v77, 0x42000000, v77
	v_mul_f32_e32 v78, 0x42000000, v78
	v_mul_f32_e32 v79, 0x42000000, v79
	v_mul_f32_e32 v80, 0x42000000, v80
	v_mul_f32_e32 v81, 0x42000000, v81
	v_cvt_pk_fp8_f32 v162, v66, v67
	v_cvt_pk_fp8_f32 v163, v70, v71
	v_cvt_pk_fp8_f32 v164, v74, v75
	v_cvt_pk_fp8_f32 v165, v78, v79
	v_cvt_pk_fp8_f32 v162, v68, v69 op_sel:[0,0,1]
	v_cvt_pk_fp8_f32 v163, v72, v73 op_sel:[0,0,1]
	v_cvt_pk_fp8_f32 v164, v76, v77 op_sel:[0,0,1]
	v_cvt_pk_fp8_f32 v165, v80, v81 op_sel:[0,0,1]
	s_waitcnt vmcnt(0)
	v_mul_f32_e32 v82, 0x42000000, v82
	v_mul_f32_e32 v83, 0x42000000, v83
	v_mul_f32_e32 v84, 0x42000000, v84
	v_mul_f32_e32 v85, 0x42000000, v85
	v_mul_f32_e32 v86, 0x42000000, v86
	v_mul_f32_e32 v87, 0x42000000, v87
	v_mul_f32_e32 v88, 0x42000000, v88
	v_mul_f32_e32 v89, 0x42000000, v89
	v_mul_f32_e32 v90, 0x42000000, v90
	v_mul_f32_e32 v91, 0x42000000, v91
	v_mul_f32_e32 v92, 0x42000000, v92
	v_mul_f32_e32 v93, 0x42000000, v93
	v_mul_f32_e32 v94, 0x42000000, v94
	v_mul_f32_e32 v95, 0x42000000, v95
	v_mul_f32_e32 v96, 0x42000000, v96
	v_mul_f32_e32 v97, 0x42000000, v97
	v_cvt_pk_fp8_f32 v166, v82, v83
	v_cvt_pk_fp8_f32 v167, v86, v87
	v_cvt_pk_fp8_f32 v168, v90, v91
	v_cvt_pk_fp8_f32 v169, v94, v95
	v_cvt_pk_fp8_f32 v166, v84, v85 op_sel:[0,0,1]
	v_cvt_pk_fp8_f32 v167, v88, v89 op_sel:[0,0,1]
	v_cvt_pk_fp8_f32 v168, v92, v93 op_sel:[0,0,1]
	v_cvt_pk_fp8_f32 v169, v96, v97 op_sel:[0,0,1]
	s_mov_b32 vcc_lo, 0xaaaaaaaa
	s_mov_b32 vcc_hi, 0xaaaaaaaa
	s_nop 1
	v_cndmask_b32_dpp v170, v154, v158, vcc quad_perm:[1,0,3,2] row_mask:0xf bank_mask:0xf
	v_cndmask_b32_dpp v174, v162, v166, vcc quad_perm:[1,0,3,2] row_mask:0xf bank_mask:0xf
	v_cndmask_b32_dpp v171, v155, v159, vcc quad_perm:[1,0,3,2] row_mask:0xf bank_mask:0xf
	v_cndmask_b32_dpp v175, v163, v167, vcc quad_perm:[1,0,3,2] row_mask:0xf bank_mask:0xf
	v_cndmask_b32_dpp v172, v156, v160, vcc quad_perm:[1,0,3,2] row_mask:0xf bank_mask:0xf
	v_cndmask_b32_dpp v176, v164, v168, vcc quad_perm:[1,0,3,2] row_mask:0xf bank_mask:0xf
	v_cndmask_b32_dpp v173, v157, v161, vcc quad_perm:[1,0,3,2] row_mask:0xf bank_mask:0xf
	v_cndmask_b32_dpp v177, v165, v169, vcc quad_perm:[1,0,3,2] row_mask:0xf bank_mask:0xf
	s_mov_b32 vcc_lo, 0x55555555
	s_mov_b32 vcc_hi, 0x55555555
	s_nop 1
	v_cndmask_b32_dpp v154, v158, v154, vcc quad_perm:[1,0,3,2] row_mask:0xf bank_mask:0xf
	v_cndmask_b32_dpp v162, v166, v162, vcc quad_perm:[1,0,3,2] row_mask:0xf bank_mask:0xf
	v_cndmask_b32_dpp v155, v159, v155, vcc quad_perm:[1,0,3,2] row_mask:0xf bank_mask:0xf
	v_cndmask_b32_dpp v163, v167, v163, vcc quad_perm:[1,0,3,2] row_mask:0xf bank_mask:0xf
	v_cndmask_b32_dpp v156, v160, v156, vcc quad_perm:[1,0,3,2] row_mask:0xf bank_mask:0xf
	v_cndmask_b32_dpp v164, v168, v164, vcc quad_perm:[1,0,3,2] row_mask:0xf bank_mask:0xf
	v_cndmask_b32_dpp v157, v161, v157, vcc quad_perm:[1,0,3,2] row_mask:0xf bank_mask:0xf
	v_cndmask_b32_dpp v165, v169, v165, vcc quad_perm:[1,0,3,2] row_mask:0xf bank_mask:0xf
	s_mov_b32 vcc_lo, 0xcccccccc
	s_mov_b32 vcc_hi, 0xcccccccc
	s_nop 1
	v_cndmask_b32_dpp v158, v154, v162, vcc quad_perm:[2,3,0,1] row_mask:0xf bank_mask:0xf
	v_cndmask_b32_dpp v166, v170, v174, vcc quad_perm:[2,3,0,1] row_mask:0xf bank_mask:0xf
	v_cndmask_b32_dpp v159, v155, v163, vcc quad_perm:[2,3,0,1] row_mask:0xf bank_mask:0xf
	v_cndmask_b32_dpp v167, v171, v175, vcc quad_perm:[2,3,0,1] row_mask:0xf bank_mask:0xf
	v_cndmask_b32_dpp v160, v156, v164, vcc quad_perm:[2,3,0,1] row_mask:0xf bank_mask:0xf
	v_cndmask_b32_dpp v168, v172, v176, vcc quad_perm:[2,3,0,1] row_mask:0xf bank_mask:0xf
	v_cndmask_b32_dpp v161, v157, v165, vcc quad_perm:[2,3,0,1] row_mask:0xf bank_mask:0xf
	v_cndmask_b32_dpp v169, v173, v177, vcc quad_perm:[2,3,0,1] row_mask:0xf bank_mask:0xf
	s_mov_b32 vcc_lo, 0x33333333
	s_mov_b32 vcc_hi, 0x33333333
	s_nop 1
	v_cndmask_b32_dpp v154, v162, v154, vcc quad_perm:[2,3,0,1] row_mask:0xf bank_mask:0xf
	v_cndmask_b32_dpp v170, v174, v170, vcc quad_perm:[2,3,0,1] row_mask:0xf bank_mask:0xf
	v_cndmask_b32_dpp v155, v163, v155, vcc quad_perm:[2,3,0,1] row_mask:0xf bank_mask:0xf
	v_cndmask_b32_dpp v171, v175, v171, vcc quad_perm:[2,3,0,1] row_mask:0xf bank_mask:0xf
	v_cndmask_b32_dpp v156, v164, v156, vcc quad_perm:[2,3,0,1] row_mask:0xf bank_mask:0xf
	v_cndmask_b32_dpp v172, v176, v172, vcc quad_perm:[2,3,0,1] row_mask:0xf bank_mask:0xf
	v_cndmask_b32_dpp v157, v165, v157, vcc quad_perm:[2,3,0,1] row_mask:0xf bank_mask:0xf
	v_cndmask_b32_dpp v173, v177, v173, vcc quad_perm:[2,3,0,1] row_mask:0xf bank_mask:0xf
	global_store_dwordx4 v179, v[154:157], s[70:71] nt
	global_store_dwordx4 v180, v[170:173], s[70:71] nt
	global_store_dwordx4 v181, v[158:161], s[70:71] nt
	global_store_dwordx4 v190, v[166:169], s[70:71] nt
	s_lshl_b32 s23, s74, 3
	s_add_i32 s98, s98, s23

.Lp2w_go_b:
	v_readlane_b32 s62, v239, 44
	v_readlane_b32 s63, v239, 45
	s_add_u32 s100, s82, s30
	s_addc_u32 s101, s83, 0
	s_add_u32 s70, s62, s31
	s_addc_u32 s71, s63, 0
	global_load_dword v34, v178, s[100:101] nt
	s_add_u32 s100, s100, s97
	s_addc_u32 s101, s101, 0
	global_load_dword v35, v178, s[100:101] nt
	s_add_u32 s100, s100, s97
	s_addc_u32 s101, s101, 0
	global_load_dword v36, v178, s[100:101] nt
	s_add_u32 s100, s100, s97
	s_addc_u32 s101, s101, 0
	global_load_dword v37, v178, s[100:101] nt
	s_add_u32 s100, s100, s97
	s_addc_u32 s101, s101, 0
	global_load_dword v38, v178, s[100:101] nt
	s_add_u32 s100, s100, s97
	s_addc_u32 s101, s101, 0
	global_load_dword v39, v178, s[100:101] nt
	s_add_u32 s100, s100, s97
	s_addc_u32 s101, s101, 0
	global_load_dword v40, v178, s[100:101] nt
	s_add_u32 s100, s100, s97
	s_addc_u32 s101, s101, 0
	global_load_dword v41, v178, s[100:101] nt
	s_add_u32 s100, s100, s97
	s_addc_u32 s101, s101, 0
	global_load_dword v42, v178, s[100:101] nt
	s_add_u32 s100, s100, s97
	s_addc_u32 s101, s101, 0
	global_load_dword v43, v178, s[100:101] nt
	s_add_u32 s100, s100, s97
	s_addc_u32 s101, s101, 0
	global_load_dword v44, v178, s[100:101] nt
	s_add_u32 s100, s100, s97
	s_addc_u32 s101, s101, 0
	global_load_dword v45, v178, s[100:101] nt
	s_add_u32 s100, s100, s97
	s_addc_u32 s101, s101, 0
	global_load_dword v46, v178, s[100:101] nt
	s_add_u32 s100, s100, s97
	s_addc_u32 s101, s101, 0
	global_load_dword v47, v178, s[100:101] nt
	s_add_u32 s100, s100, s97
	s_addc_u32 s101, s101, 0
	global_load_dword v48, v178, s[100:101] nt
	s_add_u32 s100, s100, s97
	s_addc_u32 s101, s101, 0
	global_load_dword v49, v178, s[100:101] nt
	s_add_u32 s100, s100, s97
	s_addc_u32 s101, s101, 0
	global_load_dword v50, v178, s[100:101] nt
	s_add_u32 s100, s100, s97
	s_addc_u32 s101, s101, 0
	global_load_dword v51, v178, s[100:101] nt
	s_add_u32 s100, s100, s97
	s_addc_u32 s101, s101, 0
	global_load_dword v52, v178, s[100:101] nt
	s_add_u32 s100, s100, s97
	s_addc_u32 s101, s101, 0
	global_load_dword v53, v178, s[100:101] nt
	s_add_u32 s100, s100, s97
	s_addc_u32 s101, s101, 0
	global_load_dword v54, v178, s[100:101] nt
	s_add_u32 s100, s100, s97
	s_addc_u32 s101, s101, 0
	global_load_dword v55, v178, s[100:101] nt
	s_add_u32 s100, s100, s97
	s_addc_u32 s101, s101, 0
	global_load_dword v56, v178, s[100:101] nt
	s_add_u32 s100, s100, s97
	s_addc_u32 s101, s101, 0
	global_load_dword v57, v178, s[100:101] nt
	s_add_u32 s100, s100, s97
	s_addc_u32 s101, s101, 0
	global_load_dword v58, v178, s[100:101] nt
	s_add_u32 s100, s100, s97
	s_addc_u32 s101, s101, 0
	global_load_dword v59, v178, s[100:101] nt
	s_add_u32 s100, s100, s97
	s_addc_u32 s101, s101, 0
	global_load_dword v60, v178, s[100:101] nt
	s_add_u32 s100, s100, s97
	s_addc_u32 s101, s101, 0
	global_load_dword v61, v178, s[100:101] nt
	s_add_u32 s100, s100, s97
	s_addc_u32 s101, s101, 0
	global_load_dword v62, v178, s[100:101] nt
	s_add_u32 s100, s100, s97
	s_addc_u32 s101, s101, 0
	global_load_dword v63, v178, s[100:101] nt
	s_add_u32 s100, s100, s97
	s_addc_u32 s101, s101, 0
	global_load_dword v64, v178, s[100:101] nt
	s_add_u32 s100, s100, s97
	s_addc_u32 s101, s101, 0
	global_load_dword v65, v178, s[100:101] nt
	s_add_u32 s100, s100, s97
	s_addc_u32 s101, s101, 0
	global_load_dword v66, v178, s[100:101] nt
	s_add_u32 s100, s100, s97
	s_addc_u32 s101, s101, 0
	global_load_dword v67, v178, s[100:101] nt
	s_add_u32 s100, s100, s97
	s_addc_u32 s101, s101, 0
	global_load_dword v68, v178, s[100:101] nt
	s_add_u32 s100, s100, s97
	s_addc_u32 s101, s101, 0
	global_load_dword v69, v178, s[100:101] nt
	s_add_u32 s100, s100, s97
	s_addc_u32 s101, s101, 0
	global_load_dword v70, v178, s[100:101] nt
	s_add_u32 s100, s100, s97
	s_addc_u32 s101, s101, 0
	global_load_dword v71, v178, s[100:101] nt
	s_add_u32 s100, s100, s97
	s_addc_u32 s101, s101, 0
	global_load_dword v72, v178, s[100:101] nt
	s_add_u32 s100, s100, s97
	s_addc_u32 s101, s101, 0
	global_load_dword v73, v178, s[100:101] nt
	s_add_u32 s100, s100, s97
	s_addc_u32 s101, s101, 0
	global_load_dword v74, v178, s[100:101] nt
	s_add_u32 s100, s100, s97
	s_addc_u32 s101, s101, 0
	global_load_dword v75, v178, s[100:101] nt
	s_add_u32 s100, s100, s97
	s_addc_u32 s101, s101, 0
	global_load_dword v76, v178, s[100:101] nt
	s_add_u32 s100, s100, s97
	s_addc_u32 s101, s101, 0
	global_load_dword v77, v178, s[100:101] nt
	s_add_u32 s100, s100, s97
	s_addc_u32 s101, s101, 0
	global_load_dword v78, v178, s[100:101] nt
	s_add_u32 s100, s100, s97
	s_addc_u32 s101, s101, 0
	global_load_dword v79, v178, s[100:101] nt
	s_add_u32 s100, s100, s97
	s_addc_u32 s101, s101, 0
	global_load_dword v80, v178, s[100:101] nt
	s_add_u32 s100, s100, s97
	s_addc_u32 s101, s101, 0
	global_load_dword v81, v178, s[100:101] nt
	s_add_u32 s100, s100, s97
	s_addc_u32 s101, s101, 0
	global_load_dword v82, v178, s[100:101] nt
	s_add_u32 s100, s100, s97
	s_addc_u32 s101, s101, 0
	global_load_dword v83, v178, s[100:101] nt
	s_add_u32 s100, s100, s97
	s_addc_u32 s101, s101, 0
	global_load_dword v84, v178, s[100:101] nt
	s_add_u32 s100, s100, s97
	s_addc_u32 s101, s101, 0
	global_load_dword v85, v178, s[100:101] nt
	s_add_u32 s100, s100, s97
	s_addc_u32 s101, s101, 0
	global_load_dword v86, v178, s[100:101] nt
	s_add_u32 s100, s100, s97
	s_addc_u32 s101, s101, 0
	global_load_dword v87, v178, s[100:101] nt
	s_add_u32 s100, s100, s97
	s_addc_u32 s101, s101, 0
	global_load_dword v88, v178, s[100:101] nt
	s_add_u32 s100, s100, s97
	s_addc_u32 s101, s101, 0
	global_load_dword v89, v178, s[100:101] nt
	s_add_u32 s100, s100, s97
	s_addc_u32 s101, s101, 0
	global_load_dword v90, v178, s[100:101] nt
	s_add_u32 s100, s100, s97
	s_addc_u32 s101, s101, 0
	global_load_dword v91, v178, s[100:101] nt
	s_add_u32 s100, s100, s97
	s_addc_u32 s101, s101, 0
	global_load_dword v92, v178, s[100:101] nt
	s_add_u32 s100, s100, s97
	s_addc_u32 s101, s101, 0
	global_load_dword v93, v178, s[100:101] nt
	s_add_u32 s100, s100, s97
	s_addc_u32 s101, s101, 0
	global_load_dword v94, v178, s[100:101] nt
	s_add_u32 s100, s100, s97
	s_addc_u32 s101, s101, 0
	global_load_dword v95, v178, s[100:101] nt
	s_add_u32 s100, s100, s97
	s_addc_u32 s101, s101, 0
	global_load_dword v96, v178, s[100:101] nt
	s_add_u32 s100, s100, s97
	s_addc_u32 s101, s101, 0
	s_waitcnt vmcnt(63)
	global_load_dword v97, v178, s[100:101] nt
	s_add_u32 s100, s100, s97
	s_addc_u32 s101, s101, 0
	s_waitcnt vmcnt(48)
	v_mul_f32_e32 v34, 0x42000000, v34
	v_mul_f32_e32 v35, 0x42000000, v35
	v_mul_f32_e32 v36, 0x42000000, v36
	v_mul_f32_e32 v37, 0x42000000, v37
	v_mul_f32_e32 v38, 0x42000000, v38
	v_mul_f32_e32 v39, 0x42000000, v39
	v_mul_f32_e32 v40, 0x42000000, v40
	v_mul_f32_e32 v41, 0x42000000, v41
	v_mul_f32_e32 v42, 0x42000000, v42
	v_mul_f32_e32 v43, 0x42000000, v43
	v_mul_f32_e32 v44, 0x42000000, v44
	v_mul_f32_e32 v45, 0x42000000, v45
	v_mul_f32_e32 v46, 0x42000000, v46
	v_mul_f32_e32 v47, 0x42000000, v47
	v_mul_f32_e32 v48, 0x42000000, v48
	v_mul_f32_e32 v49, 0x42000000, v49
	v_cvt_pk_fp8_f32 v154, v34, v35
	v_cvt_pk_fp8_f32 v155, v38, v39
	v_cvt_pk_fp8_f32 v156, v42, v43
	v_cvt_pk_fp8_f32 v157, v46, v47
	v_cvt_pk_fp8_f32 v154, v36, v37 op_sel:[0,0,1]
	v_cvt_pk_fp8_f32 v155, v40, v41 op_sel:[0,0,1]
	v_cvt_pk_fp8_f32 v156, v44, v45 op_sel:[0,0,1]
	v_cvt_pk_fp8_f32 v157, v48, v49 op_sel:[0,0,1]
	s_waitcnt vmcnt(32)
	v_mul_f32_e32 v50, 0x42000000, v50
	v_mul_f32_e32 v51, 0x42000000, v51
	v_mul_f32_e32 v52, 0x42000000, v52
	v_mul_f32_e32 v53, 0x42000000, v53
	v_mul_f32_e32 v54, 0x42000000, v54
	v_mul_f32_e32 v55, 0x42000000, v55
	v_mul_f32_e32 v56, 0x42000000, v56
	v_mul_f32_e32 v57, 0x42000000, v57
	v_mul_f32_e32 v58, 0x42000000, v58
	v_mul_f32_e32 v59, 0x42000000, v59
	v_mul_f32_e32 v60, 0x42000000, v60
	v_mul_f32_e32 v61, 0x42000000, v61
	v_mul_f32_e32 v62, 0x42000000, v62
	v_mul_f32_e32 v63, 0x42000000, v63
	v_mul_f32_e32 v64, 0x42000000, v64
	v_mul_f32_e32 v65, 0x42000000, v65
	v_cvt_pk_fp8_f32 v158, v50, v51
	v_cvt_pk_fp8_f32 v159, v54, v55
	v_cvt_pk_fp8_f32 v160, v58, v59
	v_cvt_pk_fp8_f32 v161, v62, v63
	v_cvt_pk_fp8_f32 v158, v52, v53 op_sel:[0,0,1]
	v_cvt_pk_fp8_f32 v159, v56, v57 op_sel:[0,0,1]
	v_cvt_pk_fp8_f32 v160, v60, v61 op_sel:[0,0,1]
	v_cvt_pk_fp8_f32 v161, v64, v65 op_sel:[0,0,1]
	s_waitcnt vmcnt(16)
	v_mul_f32_e32 v66, 0x42000000, v66
	v_mul_f32_e32 v67, 0x42000000, v67
	v_mul_f32_e32 v68, 0x42000000, v68
	v_mul_f32_e32 v69, 0x42000000, v69
	v_mul_f32_e32 v70, 0x42000000, v70
	v_mul_f32_e32 v71, 0x42000000, v71
	v_mul_f32_e32 v72, 0x42000000, v72
	v_mul_f32_e32 v73, 0x42000000, v73
	v_mul_f32_e32 v74, 0x42000000, v74
	v_mul_f32_e32 v75, 0x42000000, v75
	v_mul_f32_e32 v76, 0x42000000, v76
	v_mul_f32_e32 v77, 0x42000000, v77
	v_mul_f32_e32 v78, 0x42000000, v78
	v_mul_f32_e32 v79, 0x42000000, v79
	v_mul_f32_e32 v80, 0x42000000, v80
	v_mul_f32_e32 v81, 0x42000000, v81
	v_cvt_pk_fp8_f32 v162, v66, v67
	v_cvt_pk_fp8_f32 v163, v70, v71
	v_cvt_pk_fp8_f32 v164, v74, v75
	v_cvt_pk_fp8_f32 v165, v78, v79
	v_cvt_pk_fp8_f32 v162, v68, v69 op_sel:[0,0,1]
	v_cvt_pk_fp8_f32 v163, v72, v73 op_sel:[0,0,1]
	v_cvt_pk_fp8_f32 v164, v76, v77 op_sel:[0,0,1]
	v_cvt_pk_fp8_f32 v165, v80, v81 op_sel:[0,0,1]
	s_waitcnt vmcnt(0)
	v_mul_f32_e32 v82, 0x42000000, v82
	v_mul_f32_e32 v83, 0x42000000, v83
	v_mul_f32_e32 v84, 0x42000000, v84
	v_mul_f32_e32 v85, 0x42000000, v85
	v_mul_f32_e32 v86, 0x42000000, v86
	v_mul_f32_e32 v87, 0x42000000, v87
	v_mul_f32_e32 v88, 0x42000000, v88
	v_mul_f32_e32 v89, 0x42000000, v89
	v_mul_f32_e32 v90, 0x42000000, v90
	v_mul_f32_e32 v91, 0x42000000, v91
	v_mul_f32_e32 v92, 0x42000000, v92
	v_mul_f32_e32 v93, 0x42000000, v93
	v_mul_f32_e32 v94, 0x42000000, v94
	v_mul_f32_e32 v95, 0x42000000, v95
	v_mul_f32_e32 v96, 0x42000000, v96
	v_mul_f32_e32 v97, 0x42000000, v97
	v_cvt_pk_fp8_f32 v166, v82, v83
	v_cvt_pk_fp8_f32 v167, v86, v87
	v_cvt_pk_fp8_f32 v168, v90, v91
	v_cvt_pk_fp8_f32 v169, v94, v95
	v_cvt_pk_fp8_f32 v166, v84, v85 op_sel:[0,0,1]
	v_cvt_pk_fp8_f32 v167, v88, v89 op_sel:[0,0,1]
	v_cvt_pk_fp8_f32 v168, v92, v93 op_sel:[0,0,1]
	v_cvt_pk_fp8_f32 v169, v96, v97 op_sel:[0,0,1]
	s_mov_b32 vcc_lo, 0xaaaaaaaa
	s_mov_b32 vcc_hi, 0xaaaaaaaa
	s_nop 1
	v_cndmask_b32_dpp v170, v154, v158, vcc quad_perm:[1,0,3,2] row_mask:0xf bank_mask:0xf
	v_cndmask_b32_dpp v174, v162, v166, vcc quad_perm:[1,0,3,2] row_mask:0xf bank_mask:0xf
	v_cndmask_b32_dpp v171, v155, v159, vcc quad_perm:[1,0,3,2] row_mask:0xf bank_mask:0xf
	v_cndmask_b32_dpp v175, v163, v167, vcc quad_perm:[1,0,3,2] row_mask:0xf bank_mask:0xf
	v_cndmask_b32_dpp v172, v156, v160, vcc quad_perm:[1,0,3,2] row_mask:0xf bank_mask:0xf
	v_cndmask_b32_dpp v176, v164, v168, vcc quad_perm:[1,0,3,2] row_mask:0xf bank_mask:0xf
	v_cndmask_b32_dpp v173, v157, v161, vcc quad_perm:[1,0,3,2] row_mask:0xf bank_mask:0xf
	v_cndmask_b32_dpp v177, v165, v169, vcc quad_perm:[1,0,3,2] row_mask:0xf bank_mask:0xf
	s_mov_b32 vcc_lo, 0x55555555
	s_mov_b32 vcc_hi, 0x55555555
	s_nop 1
	v_cndmask_b32_dpp v154, v158, v154, vcc quad_perm:[1,0,3,2] row_mask:0xf bank_mask:0xf
	v_cndmask_b32_dpp v162, v166, v162, vcc quad_perm:[1,0,3,2] row_mask:0xf bank_mask:0xf
	v_cndmask_b32_dpp v155, v159, v155, vcc quad_perm:[1,0,3,2] row_mask:0xf bank_mask:0xf
	v_cndmask_b32_dpp v163, v167, v163, vcc quad_perm:[1,0,3,2] row_mask:0xf bank_mask:0xf
	v_cndmask_b32_dpp v156, v160, v156, vcc quad_perm:[1,0,3,2] row_mask:0xf bank_mask:0xf
	v_cndmask_b32_dpp v164, v168, v164, vcc quad_perm:[1,0,3,2] row_mask:0xf bank_mask:0xf
	v_cndmask_b32_dpp v157, v161, v157, vcc quad_perm:[1,0,3,2] row_mask:0xf bank_mask:0xf
	v_cndmask_b32_dpp v165, v169, v165, vcc quad_perm:[1,0,3,2] row_mask:0xf bank_mask:0xf
	s_mov_b32 vcc_lo, 0xcccccccc
	s_mov_b32 vcc_hi, 0xcccccccc
	s_nop 1
	v_cndmask_b32_dpp v158, v154, v162, vcc quad_perm:[2,3,0,1] row_mask:0xf bank_mask:0xf
	v_cndmask_b32_dpp v166, v170, v174, vcc quad_perm:[2,3,0,1] row_mask:0xf bank_mask:0xf
	v_cndmask_b32_dpp v159, v155, v163, vcc quad_perm:[2,3,0,1] row_mask:0xf bank_mask:0xf
	v_cndmask_b32_dpp v167, v171, v175, vcc quad_perm:[2,3,0,1] row_mask:0xf bank_mask:0xf
	v_cndmask_b32_dpp v160, v156, v164, vcc quad_perm:[2,3,0,1] row_mask:0xf bank_mask:0xf
	v_cndmask_b32_dpp v168, v172, v176, vcc quad_perm:[2,3,0,1] row_mask:0xf bank_mask:0xf
	v_cndmask_b32_dpp v161, v157, v165, vcc quad_perm:[2,3,0,1] row_mask:0xf bank_mask:0xf
	v_cndmask_b32_dpp v169, v173, v177, vcc quad_perm:[2,3,0,1] row_mask:0xf bank_mask:0xf
	s_mov_b32 vcc_lo, 0x33333333
	s_mov_b32 vcc_hi, 0x33333333
	s_nop 1
	v_cndmask_b32_dpp v154, v162, v154, vcc quad_perm:[2,3,0,1] row_mask:0xf bank_mask:0xf
	v_cndmask_b32_dpp v170, v174, v170, vcc quad_perm:[2,3,0,1] row_mask:0xf bank_mask:0xf
	v_cndmask_b32_dpp v155, v163, v155, vcc quad_perm:[2,3,0,1] row_mask:0xf bank_mask:0xf
	v_cndmask_b32_dpp v171, v175, v171, vcc quad_perm:[2,3,0,1] row_mask:0xf bank_mask:0xf
	v_cndmask_b32_dpp v156, v164, v156, vcc quad_perm:[2,3,0,1] row_mask:0xf bank_mask:0xf
	v_cndmask_b32_dpp v172, v176, v172, vcc quad_perm:[2,3,0,1] row_mask:0xf bank_mask:0xf
	v_cndmask_b32_dpp v157, v165, v157, vcc quad_perm:[2,3,0,1] row_mask:0xf bank_mask:0xf
	v_cndmask_b32_dpp v173, v177, v173, vcc quad_perm:[2,3,0,1] row_mask:0xf bank_mask:0xf
	global_store_dwordx4 v179, v[154:157], s[70:71] nt
	global_store_dwordx4 v180, v[170:173], s[70:71] nt
	global_store_dwordx4 v181, v[158:161], s[70:71] nt
	global_store_dwordx4 v190, v[166:169], s[70:71] nt
	s_lshl_b32 s23, s74, 3
	s_add_i32 s98, s98, s23
	s_branch .Lp2w_tail
